# MLA unit prologue: second batch of 22 loads issued before the wait for the Q loads (wait becomes vmcnt 22): one exposed load latency per unit instead of two
# speedup vs baseline: 1.0018x; 1.0018x over previous
.LBB0_1547:
	s_waitcnt lgkmcnt(0)
	v_ashrrev_i32_e32 v173, 31, v172
	v_bfe_u32 v175, v2, 5, 1
	v_lshlrev_b64 v[2:3], 6, v[172:173]
	v_mov_b64_e32 v[4:5], s[50:51]
	s_movk_i32 s2, 0xc00
	v_lshl_add_u64 v[2:3], s[54:55], 0, v[2:3]
	v_mad_i64_i32 v[4:5], s[2:3], v172, s2, v[4:5]
	global_load_dwordx4 v[66:69], v[2:3], off offset:16
	global_load_dwordx4 v[70:73], v[2:3], off
	global_load_dwordx4 v[74:77], v[2:3], off offset:32
	v_lshl_add_u64 v[2:3], v[4:5], 0, s[4:5]
	v_lshlrev_b32_e32 v98, 4, v175
	v_lshl_add_u64 v[2:3], v[2:3], 0, v[98:99]
	global_load_dwordx4 v[78:81], v[2:3], off offset:128
	global_load_dwordx4 v[82:85], v[2:3], off offset:160
	global_load_dwordx4 v[86:89], v[2:3], off offset:96
	global_load_dwordx4 v[90:93], v[2:3], off offset:64
	v_and_b32_e32 v5, 64, v214
	v_xor_b32_e32 v4, 32, v214
	v_lshlrev_b32_e32 v6, 6, v172
	v_add_u32_e32 v5, 64, v5
	v_lshlrev_b32_e32 v7, 5, v175
	v_and_b32_e32 v30, 0x3ffc0, v6
	v_cmp_lt_i32_e32 vcc, v4, v5
	v_mov_b32_e32 v179, v0
	v_cndmask_b32_e32 v98, v214, v4, vcc
	global_load_dwordx4 v[54:57], v7, s[44:45] offset:16
	global_load_dwordx4 v[62:65], v7, s[44:45]
	global_load_dwordx4 v[106:109], v[2:3], off
	global_load_dwordx4 v[94:97], v[2:3], off offset:32
	global_load_dwordx4 v[50:53], v7, s[44:45] offset:80
	global_load_dwordx4 v[58:61], v7, s[44:45] offset:64
	global_load_dwordx4 v[42:45], v7, s[44:45] offset:144
	global_load_dwordx4 v[46:49], v7, s[44:45] offset:128
	global_load_dwordx4 v[34:37], v7, s[44:45] offset:208
	global_load_dwordx4 v[38:41], v7, s[44:45] offset:192
	global_load_dwordx4 v[110:113], v7, s[44:45] offset:272
	global_load_dwordx4 v[114:117], v7, s[44:45] offset:256
	global_load_dwordx4 v[130:133], v7, s[44:45] offset:336
	global_load_dwordx4 v[134:137], v7, s[44:45] offset:320
	global_load_dwordx4 v[2:5], v30, s[46:47] offset:48
	global_load_dwordx4 v[10:13], v30, s[46:47] offset:32
	global_load_dwordx4 v[18:21], v30, s[46:47] offset:16
	global_load_dwordx4 v[26:29], v30, s[46:47]
	s_nop 0
	global_load_dwordx4 v[6:9], v30, s[48:49] offset:48
	global_load_dwordx4 v[14:17], v30, s[48:49] offset:32
	global_load_dwordx4 v[22:25], v30, s[48:49] offset:16
	s_nop 0
	global_load_dwordx4 v[30:33], v30, s[48:49]
	s_waitcnt vmcnt(22)
	v_add_f32_e32 v66, v66, v67
	v_add_f32_e32 v70, v70, v71
	v_lshlrev_b32_e32 v164, 16, v78
	v_and_b32_e32 v165, 0xffff0000, v78
	v_lshlrev_b32_e32 v166, 16, v79
	v_and_b32_e32 v167, 0xffff0000, v79
	v_lshlrev_b32_e32 v168, 16, v80
	v_and_b32_e32 v169, 0xffff0000, v80
	v_lshlrev_b32_e32 v170, 16, v81
	v_and_b32_e32 v171, 0xffff0000, v81
	v_and_b32_e32 v122, 0xffff0000, v82
	v_lshlrev_b32_e32 v123, 16, v82
	v_and_b32_e32 v138, 0xffff0000, v83
	v_lshlrev_b32_e32 v139, 16, v83
	v_and_b32_e32 v140, 0xffff0000, v84
	v_lshlrev_b32_e32 v141, 16, v84
	v_and_b32_e32 v142, 0xffff0000, v85
	v_lshlrev_b32_e32 v143, 16, v85
	v_lshlrev_b32_e32 v78, 16, v93
	v_and_b32_e32 v79, 0xffff0000, v93
	v_lshlrev_b32_e32 v80, 16, v92
	v_and_b32_e32 v81, 0xffff0000, v92
	v_lshlrev_b32_e32 v82, 16, v91
	v_and_b32_e32 v83, 0xffff0000, v91
	v_lshlrev_b32_e32 v84, 16, v90
	v_and_b32_e32 v85, 0xffff0000, v90
	v_add_f32_e32 v72, v72, v73
	v_add_f32_e32 v68, v68, v69
	v_mov_b32_e32 v71, v74
	v_mov_b32_e32 v73, v75
	v_mov_b32_e32 v67, v76
	v_mov_b32_e32 v69, v77
	v_pk_add_f32 v[74:75], v[70:71], v[72:73]
	v_pk_add_f32 v[66:67], v[66:67], v[68:69]
	v_lshlrev_b32_e32 v70, 16, v89
	v_and_b32_e32 v71, 0xffff0000, v89
	v_lshlrev_b32_e32 v72, 16, v88
	v_and_b32_e32 v73, 0xffff0000, v88
	v_pk_add_f32 v[66:67], v[74:75], v[66:67]
	v_lshlrev_b32_e32 v74, 16, v87
	v_and_b32_e32 v75, 0xffff0000, v87
	v_lshlrev_b32_e32 v76, 16, v86
	v_and_b32_e32 v77, 0xffff0000, v86
	v_pk_mul_f32 v[152:153], v[84:85], v[84:85]
	v_pk_mul_f32 v[150:151], v[82:83], v[82:83]
	v_pk_mul_f32 v[148:149], v[80:81], v[80:81]
	v_add_f32_e32 v66, v66, v67
	v_pk_mul_f32 v[146:147], v[78:79], v[78:79]
	v_fmamk_f32 v66, v66, 0x3aaaaaab, v1
	v_mul_f32_e32 v67, 0x4b800000, v66
	v_cmp_gt_f32_e32 vcc, s77, v66
	v_pk_mul_f32 v[144:145], v[76:77], v[76:77]
	v_pk_mul_f32 v[128:129], v[72:73], v[72:73]
	v_cndmask_b32_e32 v66, v66, v67, vcc
	v_rsq_f32_e32 v174, v66
	v_pk_mul_f32 v[66:67], v[74:75], v[74:75]
	v_pk_mul_f32 v[126:127], v[70:71], v[70:71]
	v_pk_mul_f32 v[68:69], v[122:123], v[122:123]
	v_pk_mul_f32 v[118:119], v[138:139], v[138:139]
	v_pk_mul_f32 v[120:121], v[140:141], v[140:141]
	v_pk_mul_f32 v[124:125], v[142:143], v[142:143]
	s_waitcnt vmcnt(19)
	v_lshlrev_b32_e32 v104, 16, v106
	v_and_b32_e32 v105, 0xffff0000, v106
	v_lshlrev_b32_e32 v102, 16, v107
	v_and_b32_e32 v103, 0xffff0000, v107
	v_pk_mul_f32 v[106:107], v[104:105], v[104:105]
	v_pk_mul_f32 v[162:163], v[102:103], v[102:103]
	v_add_f32_e32 v106, v106, v107
	v_lshlrev_b32_e32 v100, 16, v108
	v_and_b32_e32 v101, 0xffff0000, v108
	v_add_f32_e32 v106, v162, v106
	s_waitcnt vmcnt(18)
	v_lshlrev_b32_e32 v90, 16, v95
	v_and_b32_e32 v91, 0xffff0000, v95
	v_lshlrev_b32_e32 v92, 16, v94
	v_and_b32_e32 v93, 0xffff0000, v94
	v_lshlrev_b32_e32 v94, 16, v109
	v_and_b32_e32 v95, 0xffff0000, v109
	v_pk_mul_f32 v[108:109], v[100:101], v[100:101]
	v_add_f32_e32 v106, v163, v106
	v_add_f32_e32 v106, v108, v106
	v_pk_mul_f32 v[160:161], v[94:95], v[94:95]
	v_add_f32_e32 v106, v109, v106
	v_add_f32_e32 v106, v160, v106
	v_pk_mul_f32 v[158:159], v[92:93], v[92:93]
	v_add_f32_e32 v106, v161, v106
	v_add_f32_e32 v106, v158, v106
	v_pk_mul_f32 v[156:157], v[90:91], v[90:91]
	v_add_f32_e32 v106, v159, v106
	v_lshlrev_b32_e32 v88, 16, v96
	v_and_b32_e32 v89, 0xffff0000, v96
	v_add_f32_e32 v106, v156, v106
	v_lshlrev_b32_e32 v86, 16, v97
	v_and_b32_e32 v87, 0xffff0000, v97
	v_pk_mul_f32 v[96:97], v[88:89], v[88:89]
	v_add_f32_e32 v106, v157, v106
	v_add_f32_e32 v96, v96, v106
	v_pk_mul_f32 v[154:155], v[86:87], v[86:87]
	v_add_f32_e32 v96, v97, v96
	v_add_f32_e32 v96, v154, v96
	v_add_f32_e32 v96, v155, v96
	v_add_f32_e32 v96, v152, v96
	v_add_f32_e32 v96, v153, v96
	v_add_f32_e32 v96, v150, v96
	v_add_f32_e32 v96, v151, v96
	v_add_f32_e32 v96, v148, v96
	v_add_f32_e32 v96, v149, v96
	v_add_f32_e32 v96, v146, v96
	v_add_f32_e32 v96, v147, v96
	v_add_f32_e32 v96, v144, v96
	v_add_f32_e32 v96, v145, v96
	v_add_f32_e32 v66, v66, v96
	v_add_f32_e32 v66, v67, v66
	v_add_f32_e32 v66, v128, v66
	v_add_f32_e32 v66, v129, v66
	v_add_f32_e32 v66, v126, v66
	v_add_f32_e32 v66, v127, v66
	v_fmac_f32_e32 v66, v164, v164
	v_fmac_f32_e32 v66, v165, v165
	v_fmac_f32_e32 v66, v166, v166
	v_fmac_f32_e32 v66, v167, v167
	v_fmac_f32_e32 v66, v168, v168
	v_fmac_f32_e32 v66, v169, v169
	v_fmac_f32_e32 v66, v170, v170
	v_fmac_f32_e32 v66, v171, v171
	v_add_f32_e32 v66, v69, v66
	v_add_f32_e32 v66, v68, v66
	v_add_f32_e32 v66, v119, v66
	v_add_f32_e32 v66, v118, v66
	v_add_f32_e32 v66, v121, v66
	v_add_f32_e32 v66, v120, v66
	v_add_f32_e32 v66, v125, v66
	v_lshlrev_b32_e32 v98, 2, v98
	v_add_f32_e32 v66, v124, v66
	ds_bpermute_b32 v67, v98, v66
	v_mul_f32_e32 v68, 0x45800000, v174
	v_cndmask_b32_e32 v68, v174, v68, vcc
	v_mul_f32_e32 v69, v68, v68
	s_waitcnt lgkmcnt(0)
	v_add_f32_e32 v66, v66, v67
	v_mul_f32_e32 v66, v69, v66
	v_fmamk_f32 v66, v66, 0x3c2aaaab, v1
	v_mul_f32_e32 v67, 0x4b800000, v66
	v_cmp_gt_f32_e32 vcc, s77, v66
	v_readfirstlane_b32 s2, v179
	s_ashr_i32 s76, s2, 6
	v_cndmask_b32_e32 v66, v66, v67, vcc
	v_rsq_f32_e32 v66, v66
	s_cmp_lt_i32 s76, 4
	v_mul_f32_e32 v67, 0x45800000, v66
	v_cndmask_b32_e32 v66, v66, v67, vcc
	v_mul_f32_e32 v106, v68, v66
	s_waitcnt vmcnt(10)
	v_mul_f32_e32 v66, v114, v106
	v_mul_f32_e32 v129, v66, v164
	v_mul_f32_e32 v66, v110, v106
	v_mul_f32_e32 v120, v66, v168
	v_mul_f32_e32 v66, v115, v106
	v_mul_f32_e32 v127, v66, v165
	v_mul_f32_e32 v66, v111, v106
	v_mul_f32_e32 v119, v66, v169
	v_mul_f32_e32 v66, v116, v106
	v_mul_f32_e32 v126, v66, v166
	v_mul_f32_e32 v66, v112, v106
	v_mul_f32_e32 v118, v66, v170
	v_mul_f32_e32 v66, v117, v106
	v_mul_f32_e32 v125, v66, v167
	v_mul_f32_e32 v66, v113, v106
	v_mul_f32_e32 v116, v66, v171
	s_waitcnt vmcnt(8)
	v_mul_f32_e32 v66, v134, v106
	v_mul_f32_e32 v115, v66, v123
	v_mul_f32_e32 v66, v130, v106
	v_mul_f32_e32 v110, v66, v141
	v_mul_f32_e32 v66, v135, v106
	v_mul_f32_e32 v113, v66, v122
	v_mul_f32_e32 v66, v131, v106
	v_mul_f32_e32 v109, v66, v140
	v_mul_f32_e32 v66, v136, v106
	v_mul_f32_e32 v112, v66, v139
	v_mul_f32_e32 v66, v132, v106
	v_mul_f32_e32 v108, v66, v143
	v_mul_f32_e32 v66, v137, v106
	v_mul_f32_e32 v111, v66, v138
	v_mul_f32_e32 v66, v133, v106
	v_mul_f32_e32 v107, v66, v142
	ds_bpermute_b32 v138, v98, v129
	ds_bpermute_b32 v137, v98, v127
	ds_bpermute_b32 v136, v98, v126
	ds_bpermute_b32 v135, v98, v125
	ds_bpermute_b32 v134, v98, v120
	ds_bpermute_b32 v133, v98, v119
	ds_bpermute_b32 v132, v98, v118
	ds_bpermute_b32 v131, v98, v116
	ds_bpermute_b32 v130, v98, v115
	ds_bpermute_b32 v128, v98, v113
	ds_bpermute_b32 v124, v98, v112
	ds_bpermute_b32 v123, v98, v111
	ds_bpermute_b32 v122, v98, v110
	ds_bpermute_b32 v121, v98, v109
	ds_bpermute_b32 v117, v98, v108
	ds_bpermute_b32 v114, v98, v107
	s_cbranch_scc1 .LBB0_1549
	s_setprio 1
